# deferred conversion: 3 items per wave in the P5 and P14 idle slots (14.8% of the MoE conversion)
# speedup vs baseline: 1.0284x; 1.0193x over previous
; #define LAS __attribute__((address_space(3)))
; __device__ __forceinline__ int tidx() { int t = threadIdx.x; asm volatile("" : "+v"(t)); return t; }
; __device__ __forceinline__ void phase_cvt_moe(LAS unsigned char* lds, const CvtMoe a) {
;     const int tid_ = tidx(), wave = tid_ >> 6, lane = tid_ & 63;
;     LAS float* scr = (LAS float*)(lds + wave * CVT_SCR);
;     const int gw = blockIdx.x * 8 + wave, NGW = gridDim.x * 8;
;     constexpr int IG = (D / 64) * (FF / 64), ID = (FF / 64) * (D / 64);
;     for (int it = gw; it < 2 * NE * (2 * IG + ID); it += NGW) {
;         const int e = it / (2 * IG + ID); int r = it % (2 * IG + ID);
;         if (r < 2 * IG) { const int up = r / IG; r %= IG; const int nblk = FF / 64, kb = r / nblk, nb = r % nblk, n0 = nb * 64;
;             cvt_item((up ? a.wu : a.wg) + (size_t)e * D * FF, D, FF, a.gu + (size_t)e * 2 * FF * D, (n0 / 128) * 256 + up * 128 + (n0 % 128), kb * 64, n0, scr, lane); }
;         else { r -= 2 * IG; const int nblk = D / 64, kb = r / nblk, nb = r % nblk; cvt_item(a.wd + (size_t)e * FF * D, FF, D, a.dn + (size_t)e * D * FF, nb * 64, kb * 64, nb * 64, scr, lane); }
;     }
.LBB0_55:
	s_or_b64 exec, exec, s[4:5]
	s_add_u32 s4, s90, 0x30a13600
	s_addc_u32 s5, s91, 0
	v_writelane_b32 v250, s4, 6
	v_mov_b32_e32 v4, v0
	s_nop 0
	v_writelane_b32 v250, s5, 7
	s_add_u32 s4, s90, 0x46a13600
	s_addc_u32 s5, s91, 0
	v_writelane_b32 v250, s4, 8
	v_ashrrev_i32_e32 v2, 6, v4
	v_add_u32_e32 v5, s14, v2
	v_writelane_b32 v250, s5, 9
	s_mov_b32 s4, 0xe100
	v_cmp_gt_i32_e32 vcc, s4, v5
	s_and_saveexec_b64 s[4:5], vcc
	s_cbranch_execz .LBB0_62
	s_movk_i32 s6, 0x4100
	v_mul_lo_u32 v3, v2, s6
	v_add_u32_e32 v8, 0, v3
	v_lshlrev_b32_e32 v3, 2, v4
	v_bfe_u32 v6, v4, 4, 2
	v_and_b32_e32 v44, 60, v3
	v_bfe_u32 v7, v4, 3, 3
	v_lshlrev_b32_e32 v4, 3, v4
	v_lshl_add_u32 v20, v44, 2, v8
	v_mul_u32_u24_e32 v21, 0x104, v6
	v_and_b32_e32 v4, 56, v4
	v_mul_u32_u24_e32 v9, 0x104, v4
	v_lshlrev_b32_e32 v10, 2, v7
	v_lshlrev_b32_e32 v16, 2, v2
	v_add_u32_e32 v20, v20, v21
	v_mov_b32_e32 v3, 0
	v_add3_u32 v8, v8, v9, v10
	v_or_b32_e32 v9, 8, v7
	v_or_b32_e32 v10, 16, v7
	v_or_b32_e32 v11, 24, v7
	v_or_b32_e32 v12, 32, v7
	v_or_b32_e32 v13, 40, v7
	v_or_b32_e32 v14, 48, v7
	v_or_b32_e32 v15, 56, v7
	v_lshl_add_u32 v16, s2, 5, v16
	v_lshlrev_b32_e32 v17, 2, v1
	v_lshl_add_u32 v18, v2, 6, s3
	v_lshlrev_b32_e32 v19, 6, v1
	s_mov_b64 s[6:7], 0
	s_mov_b32 s3, 0x3e0f83e1
	s_movk_i32 s10, 0x57f
	s_mov_b32 s11, 0xb00000
	v_add_u32_e32 v21, 0x410, v20
	v_add_u32_e32 v22, 0x418, v20
	v_add_u32_e32 v23, 0x820, v20
	v_add_u32_e32 v24, 0x828, v20
	v_add_u32_e32 v25, 0xc30, v20
	v_add_u32_e32 v26, 0xc38, v20
	v_add_u32_e32 v27, 0x1040, v20
	v_add_u32_e32 v28, 0x1048, v20
	v_add_u32_e32 v29, 0x1450, v20
	v_add_u32_e32 v30, 0x1458, v20
	v_add_u32_e32 v31, 0x1860, v20
	v_add_u32_e32 v32, 0x1868, v20
	v_add_u32_e32 v33, 0x1c70, v20
	v_add_u32_e32 v34, 0x1c78, v20
	v_add_u32_e32 v35, 0x2080, v20
	v_add_u32_e32 v36, 0x2088, v20
	v_add_u32_e32 v37, 0x2490, v20
	v_add_u32_e32 v38, 0x2498, v20
	v_add_u32_e32 v39, 0x28a0, v20
	v_add_u32_e32 v40, 0x28a8, v20
	v_add_u32_e32 v41, 0x2cb0, v20
	v_add_u32_e32 v42, 0x2cb8, v20
	s_movk_i32 s12, 0xba3
	s_mov_b32 s13, 0xb000
	s_mov_b32 s14, 0x16000
	s_mov_b32 s15, 0x21000
	s_mov_b32 s16, 0x2c000
	s_mov_b32 s17, 0x37000
	s_mov_b32 s18, 0x42000
	s_mov_b32 s19, 0x4d000
	s_mov_b32 s20, 0x58000
	s_mov_b32 s21, 0x63000
	s_mov_b32 s22, 0x6e000
	s_mov_b32 s23, 0x79000
	s_mov_b32 s24, 0x84000
	s_mov_b32 s25, 0x8f000
	s_mov_b32 s26, 0x9a000
	s_mov_b32 s27, 0xa5000
	s_mov_b32 s28, 0xe0ff
	v_lshlrev_b32_e32 v2, 2, v44
	v_add_u32_e32 v43, 0x30c0, v20
	v_add_u32_e32 v44, 0x30c8, v20
	v_add_u32_e32 v45, 0x34d0, v20
	v_add_u32_e32 v46, 0x34d8, v20
	v_mov_b32_e32 v47, 6
	v_mov_b32_e32 v48, 1
	v_mov_b32_e32 v49, 8
	v_mov_b32_e32 v50, 7
	s_branch .LBB0_58

; #define LAS __attribute__((address_space(3)))
; __device__ __forceinline__ int tidx() { int t = threadIdx.x; asm volatile("" : "+v"(t)); return t; }
; __device__ __forceinline__ void phase_cvt_moe(LAS unsigned char* lds, const CvtMoe a) {
;     const int tid_ = tidx(), wave = tid_ >> 6, lane = tid_ & 63;
;     LAS float* scr = (LAS float*)(lds + wave * CVT_SCR);
;     const int gw = blockIdx.x * 8 + wave, NGW = gridDim.x * 8;
;     constexpr int IG = (D / 64) * (FF / 64), ID = (FF / 64) * (D / 64);
;     for (int it = gw; it < 2 * NE * (2 * IG + ID); it += NGW) {
;         const int e = it / (2 * IG + ID); int r = it % (2 * IG + ID);
;         if (r < 2 * IG) { const int up = r / IG; r %= IG; const int nblk = FF / 64, kb = r / nblk, nb = r % nblk, n0 = nb * 64;
.Lcvp5_entry:
	s_sub_i32 s0, s94, 64
	v_readlane_b32 s2, v250, 26
	v_readlane_b32 s3, v250, 27
	s_nop 3
	s_sub_u32 s2, s2, 0xc0
	s_subb_u32 s3, s3, 0
	s_load_dwordx2 s[38:39], s[2:3], 0x90
	s_load_dwordx2 s[40:41], s[2:3], 0x98
	s_load_dwordx2 s[34:35], s[2:3], 0xa0
	s_lshl_b32 s0, s0, 3
	s_add_i32 s0, s0, 0xe100
	v_mov_b32_e32 v131, 0x600
	s_waitcnt lgkmcnt(0)
	s_add_u32 s4, s90, 0x30a13600
	s_addc_u32 s5, s91, 0
	v_writelane_b32 v250, s4, 6
	v_mov_b32_e32 v130, v0
	s_nop 0
	v_writelane_b32 v250, s5, 7
	s_add_u32 s4, s90, 0x46a13600
	s_addc_u32 s5, s91, 0
	v_writelane_b32 v250, s4, 8
	v_ashrrev_i32_e32 v2, 6, v130
	v_add_u32_e32 v5, s0, v2
	v_writelane_b32 v250, s5, 9
	s_mov_b32 s4, 0xf300
	v_cmp_gt_i32_e32 vcc, s4, v5
	s_and_saveexec_b64 s[4:5], vcc
	s_cbranch_execz .Lcvp5_62
	s_movk_i32 s6, 0x4100
	v_mul_lo_u32 v3, v2, s6
	v_add_u32_e32 v8, 0, v3
	v_lshlrev_b32_e32 v3, 2, v130
	v_bfe_u32 v6, v130, 4, 2
	v_and_b32_e32 v44, 60, v3
	v_bfe_u32 v7, v130, 3, 3
	v_lshlrev_b32_e32 v130, 3, v130
	v_lshl_add_u32 v20, v44, 2, v8
	v_mul_u32_u24_e32 v21, 0x104, v6
	v_and_b32_e32 v130, 56, v130
	v_mul_u32_u24_e32 v9, 0x104, v130
	v_lshlrev_b32_e32 v10, 2, v7
	v_lshlrev_b32_e32 v16, 2, v2
	v_add_u32_e32 v20, v20, v21
	v_mov_b32_e32 v3, 0
	v_add3_u32 v8, v8, v9, v10
	v_or_b32_e32 v9, 8, v7
	v_or_b32_e32 v10, 16, v7
	v_or_b32_e32 v11, 24, v7
	v_or_b32_e32 v12, 32, v7
	v_or_b32_e32 v13, 40, v7
	v_or_b32_e32 v14, 48, v7
	v_or_b32_e32 v15, 56, v7
	v_lshlrev_b32_e32 v16, 2, v5
	v_lshlrev_b32_e32 v17, 2, v131
	v_lshlrev_b32_e32 v18, 6, v5
	v_lshlrev_b32_e32 v19, 6, v131
	s_mov_b64 s[6:7], 0
	s_mov_b32 s3, 0x3e0f83e1
	s_movk_i32 s10, 0x57f
	s_mov_b32 s11, 0xb00000
	v_add_u32_e32 v21, 0x410, v20
	v_add_u32_e32 v22, 0x418, v20
	v_add_u32_e32 v23, 0x820, v20
	v_add_u32_e32 v24, 0x828, v20
	v_add_u32_e32 v25, 0xc30, v20
	v_add_u32_e32 v26, 0xc38, v20
	v_add_u32_e32 v27, 0x1040, v20
	v_add_u32_e32 v28, 0x1048, v20
	v_add_u32_e32 v29, 0x1450, v20
	v_add_u32_e32 v30, 0x1458, v20
	v_add_u32_e32 v31, 0x1860, v20
	v_add_u32_e32 v32, 0x1868, v20
	v_add_u32_e32 v33, 0x1c70, v20
	v_add_u32_e32 v34, 0x1c78, v20
	v_add_u32_e32 v35, 0x2080, v20
	v_add_u32_e32 v36, 0x2088, v20
	v_add_u32_e32 v37, 0x2490, v20
	v_add_u32_e32 v38, 0x2498, v20
	v_add_u32_e32 v39, 0x28a0, v20
	v_add_u32_e32 v40, 0x28a8, v20
	v_add_u32_e32 v41, 0x2cb0, v20
	v_add_u32_e32 v42, 0x2cb8, v20
	s_movk_i32 s64, 0xba3
	s_mov_b32 s65, 0xb000
	s_mov_b32 s66, 0x16000
	s_mov_b32 s67, 0x21000
	s_mov_b32 s16, 0x2c000
	s_mov_b32 s68, 0x37000
	s_mov_b32 s69, 0x42000
	s_mov_b32 s19, 0x4d000
	s_mov_b32 s20, 0x58000
	s_mov_b32 s21, 0x63000
	s_mov_b32 s70, 0x6e000
	s_mov_b32 s23, 0x79000
	s_mov_b32 s24, 0x84000
	s_mov_b32 s25, 0x8f000
	s_mov_b32 s26, 0x9a000
	s_mov_b32 s27, 0xa5000
	s_mov_b32 s71, 0xf2ff
	v_lshlrev_b32_e32 v2, 2, v44
	v_add_u32_e32 v43, 0x30c0, v20
	v_add_u32_e32 v44, 0x30c8, v20
	v_add_u32_e32 v45, 0x34d0, v20
	v_add_u32_e32 v46, 0x34d8, v20
	v_mov_b32_e32 v47, 6
	v_mov_b32_e32 v132, 1
	v_mov_b32_e32 v133, 8
	v_mov_b32_e32 v134, 7
	s_branch .Lcvp5_58

; #define LAS __attribute__((address_space(3)))
; __device__ __forceinline__ int tidx() { int t = threadIdx.x; asm volatile("" : "+v"(t)); return t; }
; __device__ __forceinline__ void phase_cvt_moe(LAS unsigned char* lds, const CvtMoe a) {
;     const int tid_ = tidx(), wave = tid_ >> 6, lane = tid_ & 63;
;     LAS float* scr = (LAS float*)(lds + wave * CVT_SCR);
;     const int gw = blockIdx.x * 8 + wave, NGW = gridDim.x * 8;
;     constexpr int IG = (D / 64) * (FF / 64), ID = (FF / 64) * (D / 64);
;     for (int it = gw; it < 2 * NE * (2 * IG + ID); it += NGW) {
;         const int e = it / (2 * IG + ID); int r = it % (2 * IG + ID);
;         if (r < 2 * IG) { const int up = r / IG; r %= IG; const int nblk = FF / 64, kb = r / nblk, nb = r % nblk, n0 = nb * 64;
.Lcvp14_entry:
	s_sub_i32 s0, s94, 32
	v_readlane_b32 s2, v250, 26
	v_readlane_b32 s3, v250, 27
	s_nop 3
	s_sub_u32 s2, s2, 0xc0
	s_subb_u32 s3, s3, 0
	s_load_dwordx2 s[38:39], s[2:3], 0x90
	s_load_dwordx2 s[40:41], s[2:3], 0x98
	s_load_dwordx2 s[34:35], s[2:3], 0xa0
	s_lshl_b32 s0, s0, 3
	s_add_i32 s0, s0, 0xf300
	v_mov_b32_e32 v131, 0x700
	s_waitcnt lgkmcnt(0)
	s_add_u32 s4, s90, 0x30a13600
	s_addc_u32 s5, s91, 0
	v_writelane_b32 v250, s4, 6
	v_mov_b32_e32 v130, v0
	s_nop 0
	v_writelane_b32 v250, s5, 7
	s_add_u32 s4, s90, 0x46a13600
	s_addc_u32 s5, s91, 0
	v_writelane_b32 v250, s4, 8
	v_ashrrev_i32_e32 v2, 6, v130
	v_add_u32_e32 v5, s0, v2
	v_writelane_b32 v250, s5, 9
	s_mov_b32 s4, 0x10800
	v_cmp_gt_i32_e32 vcc, s4, v5
	s_and_saveexec_b64 s[4:5], vcc
	s_cbranch_execz .Lcvp14_62
	s_movk_i32 s6, 0x4100
	v_mul_lo_u32 v3, v2, s6
	v_add_u32_e32 v8, 0, v3
	v_lshlrev_b32_e32 v3, 2, v130
	v_bfe_u32 v6, v130, 4, 2
	v_and_b32_e32 v44, 60, v3
	v_bfe_u32 v7, v130, 3, 3
	v_lshlrev_b32_e32 v130, 3, v130
	v_lshl_add_u32 v20, v44, 2, v8
	v_mul_u32_u24_e32 v21, 0x104, v6
	v_and_b32_e32 v130, 56, v130
	v_mul_u32_u24_e32 v9, 0x104, v130
	v_lshlrev_b32_e32 v10, 2, v7
	v_lshlrev_b32_e32 v16, 2, v2
	v_add_u32_e32 v20, v20, v21
	v_mov_b32_e32 v3, 0
	v_add3_u32 v8, v8, v9, v10
	v_or_b32_e32 v9, 8, v7
	v_or_b32_e32 v10, 16, v7
	v_or_b32_e32 v11, 24, v7
	v_or_b32_e32 v12, 32, v7
	v_or_b32_e32 v13, 40, v7
	v_or_b32_e32 v14, 48, v7
	v_or_b32_e32 v15, 56, v7
	v_lshlrev_b32_e32 v16, 2, v5
	v_lshlrev_b32_e32 v17, 2, v131
	v_lshlrev_b32_e32 v18, 6, v5
	v_lshlrev_b32_e32 v19, 6, v131
	s_mov_b64 s[6:7], 0
	s_mov_b32 s3, 0x3e0f83e1
	s_movk_i32 s10, 0x57f
	s_mov_b32 s11, 0xb00000
	v_add_u32_e32 v21, 0x410, v20
	v_add_u32_e32 v22, 0x418, v20
	v_add_u32_e32 v23, 0x820, v20
	v_add_u32_e32 v24, 0x828, v20
	v_add_u32_e32 v25, 0xc30, v20
	v_add_u32_e32 v26, 0xc38, v20
	v_add_u32_e32 v27, 0x1040, v20
	v_add_u32_e32 v28, 0x1048, v20
	v_add_u32_e32 v29, 0x1450, v20
	v_add_u32_e32 v30, 0x1458, v20
	v_add_u32_e32 v31, 0x1860, v20
	v_add_u32_e32 v32, 0x1868, v20
	v_add_u32_e32 v33, 0x1c70, v20
	v_add_u32_e32 v34, 0x1c78, v20
	v_add_u32_e32 v35, 0x2080, v20
	v_add_u32_e32 v36, 0x2088, v20
	v_add_u32_e32 v37, 0x2490, v20
	v_add_u32_e32 v38, 0x2498, v20
	v_add_u32_e32 v39, 0x28a0, v20
	v_add_u32_e32 v40, 0x28a8, v20
	v_add_u32_e32 v41, 0x2cb0, v20
	v_add_u32_e32 v42, 0x2cb8, v20
	s_movk_i32 s64, 0xba3
	s_mov_b32 s65, 0xb000
	s_mov_b32 s66, 0x16000
	s_mov_b32 s67, 0x21000
	s_mov_b32 s16, 0x2c000
	s_mov_b32 s68, 0x37000
	s_mov_b32 s69, 0x42000
	s_mov_b32 s19, 0x4d000
	s_mov_b32 s20, 0x58000
	s_mov_b32 s21, 0x63000
	s_mov_b32 s70, 0x6e000
	s_mov_b32 s23, 0x79000
	s_mov_b32 s24, 0x84000
	s_mov_b32 s25, 0x8f000
	s_mov_b32 s26, 0x9a000
	s_mov_b32 s27, 0xa5000
	s_mov_b32 s71, 0x107ff
	v_lshlrev_b32_e32 v2, 2, v44
	v_add_u32_e32 v43, 0x30c0, v20
	v_add_u32_e32 v44, 0x30c8, v20
	v_add_u32_e32 v45, 0x34d0, v20
	v_add_u32_e32 v46, 0x34d8, v20
	v_mov_b32_e32 v47, 6
	v_mov_b32_e32 v132, 1
	v_mov_b32_e32 v133, 8
	v_mov_b32_e32 v134, 7
	s_branch .Lcvp14_58
